# v102 + accumulator zeroing at every GEMM unit start: 127 v_mov_b32 replaced by 63 v_pk_mov_b32 (two registers per VALU issue) in all 10 GEMM copies
# speedup vs baseline: 1.0105x; 1.0105x over previous
.LBB0_199:
	s_add_u32 s8, s34, 0x40080
	s_addc_u32 s9, s35, 0
	s_add_u32 s67, s38, 0x100
	v_mov_b32_e32 v10, 0
	v_lshl_add_u64 v[224:225], s[8:9], 0, v[220:221]
	v_lshl_add_u64 v[226:227], s[8:9], 0, v[222:223]
	s_addc_u32 s68, s39, 0
	s_mov_b32 s69, -2
	s_mov_b64 s[38:39], 0
	s_xor_b64 s[40:41], s[36:37], -1
	v_mov_b32_e32 v11, v10
	v_pk_mov_b32 v[12:13], v[10:11], v[10:11]
	v_pk_mov_b32 v[14:15], v[10:11], v[10:11]
	v_pk_mov_b32 v[16:17], v[10:11], v[10:11]
	v_pk_mov_b32 v[26:27], v[10:11], v[10:11]
	v_pk_mov_b32 v[28:29], v[10:11], v[10:11]
	v_pk_mov_b32 v[30:31], v[10:11], v[10:11]
	v_pk_mov_b32 v[32:33], v[10:11], v[10:11]
	v_pk_mov_b32 v[42:43], v[10:11], v[10:11]
	v_pk_mov_b32 v[44:45], v[10:11], v[10:11]
	v_pk_mov_b32 v[46:47], v[10:11], v[10:11]
	v_pk_mov_b32 v[48:49], v[10:11], v[10:11]
	v_pk_mov_b32 v[58:59], v[10:11], v[10:11]
	v_pk_mov_b32 v[60:61], v[10:11], v[10:11]
	v_pk_mov_b32 v[62:63], v[10:11], v[10:11]
	v_pk_mov_b32 v[64:65], v[10:11], v[10:11]
	v_pk_mov_b32 v[18:19], v[10:11], v[10:11]
	v_pk_mov_b32 v[20:21], v[10:11], v[10:11]
	v_pk_mov_b32 v[22:23], v[10:11], v[10:11]
	v_pk_mov_b32 v[24:25], v[10:11], v[10:11]
	v_pk_mov_b32 v[34:35], v[10:11], v[10:11]
	v_pk_mov_b32 v[36:37], v[10:11], v[10:11]
	v_pk_mov_b32 v[38:39], v[10:11], v[10:11]
	v_pk_mov_b32 v[40:41], v[10:11], v[10:11]
	v_pk_mov_b32 v[50:51], v[10:11], v[10:11]
	v_pk_mov_b32 v[52:53], v[10:11], v[10:11]
	v_pk_mov_b32 v[54:55], v[10:11], v[10:11]
	v_pk_mov_b32 v[56:57], v[10:11], v[10:11]
	v_pk_mov_b32 v[68:69], v[10:11], v[10:11]
	v_pk_mov_b32 v[70:71], v[10:11], v[10:11]
	v_pk_mov_b32 v[72:73], v[10:11], v[10:11]
	v_pk_mov_b32 v[74:75], v[10:11], v[10:11]
	v_pk_mov_b32 v[76:77], v[10:11], v[10:11]
	v_pk_mov_b32 v[78:79], v[10:11], v[10:11]
	v_pk_mov_b32 v[80:81], v[10:11], v[10:11]
	v_pk_mov_b32 v[82:83], v[10:11], v[10:11]
	v_pk_mov_b32 v[92:93], v[10:11], v[10:11]
	v_pk_mov_b32 v[94:95], v[10:11], v[10:11]
	v_pk_mov_b32 v[96:97], v[10:11], v[10:11]
	v_pk_mov_b32 v[98:99], v[10:11], v[10:11]
	v_pk_mov_b32 v[108:109], v[10:11], v[10:11]
	v_pk_mov_b32 v[110:111], v[10:11], v[10:11]
	v_pk_mov_b32 v[112:113], v[10:11], v[10:11]
	v_pk_mov_b32 v[114:115], v[10:11], v[10:11]
	v_pk_mov_b32 v[124:125], v[10:11], v[10:11]
	v_pk_mov_b32 v[126:127], v[10:11], v[10:11]
	v_pk_mov_b32 v[128:129], v[10:11], v[10:11]
	v_pk_mov_b32 v[130:131], v[10:11], v[10:11]
	v_pk_mov_b32 v[84:85], v[10:11], v[10:11]
	v_pk_mov_b32 v[86:87], v[10:11], v[10:11]
	v_pk_mov_b32 v[88:89], v[10:11], v[10:11]
	v_pk_mov_b32 v[90:91], v[10:11], v[10:11]
	v_pk_mov_b32 v[100:101], v[10:11], v[10:11]
	v_pk_mov_b32 v[102:103], v[10:11], v[10:11]
	v_pk_mov_b32 v[104:105], v[10:11], v[10:11]
	v_pk_mov_b32 v[106:107], v[10:11], v[10:11]
	v_pk_mov_b32 v[116:117], v[10:11], v[10:11]
	v_pk_mov_b32 v[118:119], v[10:11], v[10:11]
	v_pk_mov_b32 v[120:121], v[10:11], v[10:11]
	v_pk_mov_b32 v[122:123], v[10:11], v[10:11]
	v_pk_mov_b32 v[132:133], v[10:11], v[10:11]
	v_pk_mov_b32 v[134:135], v[10:11], v[10:11]
	v_pk_mov_b32 v[136:137], v[10:11], v[10:11]
	v_pk_mov_b32 v[138:139], v[10:11], v[10:11]
	s_branch .LBB0_201

.LBB0_482:
	v_mov_b32_e32 v2, 0
	s_mov_b32 s8, 0
	s_mov_b64 s[36:37], -1
	s_mov_b64 s[58:59], 0
	v_mov_b32_e32 v3, v2
	v_pk_mov_b32 v[4:5], v[2:3], v[2:3]
	v_pk_mov_b32 v[6:7], v[2:3], v[2:3]
	v_pk_mov_b32 v[8:9], v[2:3], v[2:3]
	v_pk_mov_b32 v[18:19], v[2:3], v[2:3]
	v_pk_mov_b32 v[20:21], v[2:3], v[2:3]
	v_pk_mov_b32 v[22:23], v[2:3], v[2:3]
	v_pk_mov_b32 v[24:25], v[2:3], v[2:3]
	v_pk_mov_b32 v[34:35], v[2:3], v[2:3]
	v_pk_mov_b32 v[36:37], v[2:3], v[2:3]
	v_pk_mov_b32 v[38:39], v[2:3], v[2:3]
	v_pk_mov_b32 v[40:41], v[2:3], v[2:3]
	v_pk_mov_b32 v[50:51], v[2:3], v[2:3]
	v_pk_mov_b32 v[52:53], v[2:3], v[2:3]
	v_pk_mov_b32 v[54:55], v[2:3], v[2:3]
	v_pk_mov_b32 v[56:57], v[2:3], v[2:3]
	v_pk_mov_b32 v[10:11], v[2:3], v[2:3]
	v_pk_mov_b32 v[12:13], v[2:3], v[2:3]
	v_pk_mov_b32 v[14:15], v[2:3], v[2:3]
	v_pk_mov_b32 v[16:17], v[2:3], v[2:3]
	v_pk_mov_b32 v[26:27], v[2:3], v[2:3]
	v_pk_mov_b32 v[28:29], v[2:3], v[2:3]
	v_pk_mov_b32 v[30:31], v[2:3], v[2:3]
	v_pk_mov_b32 v[32:33], v[2:3], v[2:3]
	v_pk_mov_b32 v[42:43], v[2:3], v[2:3]
	v_pk_mov_b32 v[44:45], v[2:3], v[2:3]
	v_pk_mov_b32 v[46:47], v[2:3], v[2:3]
	v_pk_mov_b32 v[48:49], v[2:3], v[2:3]
	v_pk_mov_b32 v[58:59], v[2:3], v[2:3]
	v_pk_mov_b32 v[60:61], v[2:3], v[2:3]
	v_pk_mov_b32 v[62:63], v[2:3], v[2:3]
	v_pk_mov_b32 v[64:65], v[2:3], v[2:3]
	v_pk_mov_b32 v[68:69], v[2:3], v[2:3]
	v_pk_mov_b32 v[70:71], v[2:3], v[2:3]
	v_pk_mov_b32 v[72:73], v[2:3], v[2:3]
	v_pk_mov_b32 v[74:75], v[2:3], v[2:3]
	v_pk_mov_b32 v[84:85], v[2:3], v[2:3]
	v_pk_mov_b32 v[86:87], v[2:3], v[2:3]
	v_pk_mov_b32 v[88:89], v[2:3], v[2:3]
	v_pk_mov_b32 v[90:91], v[2:3], v[2:3]
	v_pk_mov_b32 v[100:101], v[2:3], v[2:3]
	v_pk_mov_b32 v[102:103], v[2:3], v[2:3]
	v_pk_mov_b32 v[104:105], v[2:3], v[2:3]
	v_pk_mov_b32 v[106:107], v[2:3], v[2:3]
	v_pk_mov_b32 v[116:117], v[2:3], v[2:3]
	v_pk_mov_b32 v[118:119], v[2:3], v[2:3]
	v_pk_mov_b32 v[120:121], v[2:3], v[2:3]
	v_pk_mov_b32 v[122:123], v[2:3], v[2:3]
	v_pk_mov_b32 v[76:77], v[2:3], v[2:3]
	v_pk_mov_b32 v[78:79], v[2:3], v[2:3]
	v_pk_mov_b32 v[80:81], v[2:3], v[2:3]
	v_pk_mov_b32 v[82:83], v[2:3], v[2:3]
	v_pk_mov_b32 v[92:93], v[2:3], v[2:3]
	v_pk_mov_b32 v[94:95], v[2:3], v[2:3]
	v_pk_mov_b32 v[96:97], v[2:3], v[2:3]
	v_pk_mov_b32 v[98:99], v[2:3], v[2:3]
	v_pk_mov_b32 v[108:109], v[2:3], v[2:3]
	v_pk_mov_b32 v[110:111], v[2:3], v[2:3]
	v_pk_mov_b32 v[112:113], v[2:3], v[2:3]
	v_pk_mov_b32 v[114:115], v[2:3], v[2:3]
	v_pk_mov_b32 v[124:125], v[2:3], v[2:3]
	v_pk_mov_b32 v[126:127], v[2:3], v[2:3]
	v_pk_mov_b32 v[128:129], v[2:3], v[2:3]
	v_pk_mov_b32 v[130:131], v[2:3], v[2:3]
	s_branch .LBB0_484

.LBB0_506:
	s_add_u32 s8, s46, 0x40080
	s_addc_u32 s9, s47, 0
	s_add_u32 s89, s36, 0x100
	v_mov_b32_e32 v2, 0
	v_lshl_add_u64 v[212:213], s[8:9], 0, v[208:209]
	v_lshl_add_u64 v[214:215], s[8:9], 0, v[210:211]
	s_addc_u32 s90, s37, 0
	s_mov_b32 s91, -2
	s_mov_b64 s[48:49], 0
	s_xor_b64 s[50:51], s[50:51], -1
	v_mov_b32_e32 v3, v2
	v_pk_mov_b32 v[4:5], v[2:3], v[2:3]
	v_pk_mov_b32 v[6:7], v[2:3], v[2:3]
	v_pk_mov_b32 v[8:9], v[2:3], v[2:3]
	v_pk_mov_b32 v[10:11], v[2:3], v[2:3]
	v_pk_mov_b32 v[12:13], v[2:3], v[2:3]
	v_pk_mov_b32 v[18:19], v[2:3], v[2:3]
	v_pk_mov_b32 v[20:21], v[2:3], v[2:3]
	v_pk_mov_b32 v[26:27], v[2:3], v[2:3]
	v_pk_mov_b32 v[28:29], v[2:3], v[2:3]
	v_pk_mov_b32 v[34:35], v[2:3], v[2:3]
	v_pk_mov_b32 v[36:37], v[2:3], v[2:3]
	v_pk_mov_b32 v[42:43], v[2:3], v[2:3]
	v_pk_mov_b32 v[44:45], v[2:3], v[2:3]
	v_pk_mov_b32 v[50:51], v[2:3], v[2:3]
	v_pk_mov_b32 v[52:53], v[2:3], v[2:3]
	v_pk_mov_b32 v[14:15], v[2:3], v[2:3]
	v_pk_mov_b32 v[16:17], v[2:3], v[2:3]
	v_pk_mov_b32 v[22:23], v[2:3], v[2:3]
	v_pk_mov_b32 v[24:25], v[2:3], v[2:3]
	v_pk_mov_b32 v[30:31], v[2:3], v[2:3]
	v_pk_mov_b32 v[32:33], v[2:3], v[2:3]
	v_pk_mov_b32 v[38:39], v[2:3], v[2:3]
	v_pk_mov_b32 v[40:41], v[2:3], v[2:3]
	v_pk_mov_b32 v[46:47], v[2:3], v[2:3]
	v_pk_mov_b32 v[48:49], v[2:3], v[2:3]
	v_pk_mov_b32 v[54:55], v[2:3], v[2:3]
	v_pk_mov_b32 v[56:57], v[2:3], v[2:3]
	v_pk_mov_b32 v[58:59], v[2:3], v[2:3]
	v_pk_mov_b32 v[60:61], v[2:3], v[2:3]
	v_pk_mov_b32 v[62:63], v[2:3], v[2:3]
	v_pk_mov_b32 v[64:65], v[2:3], v[2:3]
	v_pk_mov_b32 v[68:69], v[2:3], v[2:3]
	v_pk_mov_b32 v[70:71], v[2:3], v[2:3]
	v_pk_mov_b32 v[72:73], v[2:3], v[2:3]
	v_pk_mov_b32 v[74:75], v[2:3], v[2:3]
	v_pk_mov_b32 v[76:77], v[2:3], v[2:3]
	v_pk_mov_b32 v[78:79], v[2:3], v[2:3]
	v_pk_mov_b32 v[84:85], v[2:3], v[2:3]
	v_pk_mov_b32 v[86:87], v[2:3], v[2:3]
	v_pk_mov_b32 v[92:93], v[2:3], v[2:3]
	v_pk_mov_b32 v[94:95], v[2:3], v[2:3]
	v_pk_mov_b32 v[100:101], v[2:3], v[2:3]
	v_pk_mov_b32 v[102:103], v[2:3], v[2:3]
	v_pk_mov_b32 v[108:109], v[2:3], v[2:3]
	v_pk_mov_b32 v[110:111], v[2:3], v[2:3]
	v_pk_mov_b32 v[116:117], v[2:3], v[2:3]
	v_pk_mov_b32 v[118:119], v[2:3], v[2:3]
	v_pk_mov_b32 v[80:81], v[2:3], v[2:3]
	v_pk_mov_b32 v[82:83], v[2:3], v[2:3]
	v_pk_mov_b32 v[88:89], v[2:3], v[2:3]
	v_pk_mov_b32 v[90:91], v[2:3], v[2:3]
	v_pk_mov_b32 v[96:97], v[2:3], v[2:3]
	v_pk_mov_b32 v[98:99], v[2:3], v[2:3]
	v_pk_mov_b32 v[104:105], v[2:3], v[2:3]
	v_pk_mov_b32 v[106:107], v[2:3], v[2:3]
	v_pk_mov_b32 v[112:113], v[2:3], v[2:3]
	v_pk_mov_b32 v[114:115], v[2:3], v[2:3]
	v_pk_mov_b32 v[120:121], v[2:3], v[2:3]
	v_pk_mov_b32 v[122:123], v[2:3], v[2:3]
	v_pk_mov_b32 v[124:125], v[2:3], v[2:3]
	v_pk_mov_b32 v[126:127], v[2:3], v[2:3]
	v_pk_mov_b32 v[128:129], v[2:3], v[2:3]
	v_pk_mov_b32 v[130:131], v[2:3], v[2:3]
	s_branch .LBB0_508

.LBB0_677:
	s_add_u32 s8, s46, 0x40080
	s_addc_u32 s9, s47, 0
	s_add_u32 s89, s36, 0x100
	v_mov_b32_e32 v2, 0
	v_lshl_add_u64 v[210:211], s[8:9], 0, v[202:203]
	v_lshl_add_u64 v[212:213], s[8:9], 0, v[208:209]
	s_addc_u32 s90, s37, 0
	s_mov_b32 s91, -2
	s_mov_b64 s[48:49], 0
	s_xor_b64 s[50:51], s[50:51], -1
	v_mov_b32_e32 v3, v2
	v_pk_mov_b32 v[4:5], v[2:3], v[2:3]
	v_pk_mov_b32 v[6:7], v[2:3], v[2:3]
	v_pk_mov_b32 v[8:9], v[2:3], v[2:3]
	v_pk_mov_b32 v[10:11], v[2:3], v[2:3]
	v_pk_mov_b32 v[12:13], v[2:3], v[2:3]
	v_pk_mov_b32 v[18:19], v[2:3], v[2:3]
	v_pk_mov_b32 v[20:21], v[2:3], v[2:3]
	v_pk_mov_b32 v[26:27], v[2:3], v[2:3]
	v_pk_mov_b32 v[28:29], v[2:3], v[2:3]
	v_pk_mov_b32 v[34:35], v[2:3], v[2:3]
	v_pk_mov_b32 v[36:37], v[2:3], v[2:3]
	v_pk_mov_b32 v[42:43], v[2:3], v[2:3]
	v_pk_mov_b32 v[44:45], v[2:3], v[2:3]
	v_pk_mov_b32 v[50:51], v[2:3], v[2:3]
	v_pk_mov_b32 v[52:53], v[2:3], v[2:3]
	v_pk_mov_b32 v[14:15], v[2:3], v[2:3]
	v_pk_mov_b32 v[16:17], v[2:3], v[2:3]
	v_pk_mov_b32 v[22:23], v[2:3], v[2:3]
	v_pk_mov_b32 v[24:25], v[2:3], v[2:3]
	v_pk_mov_b32 v[30:31], v[2:3], v[2:3]
	v_pk_mov_b32 v[32:33], v[2:3], v[2:3]
	v_pk_mov_b32 v[38:39], v[2:3], v[2:3]
	v_pk_mov_b32 v[40:41], v[2:3], v[2:3]
	v_pk_mov_b32 v[46:47], v[2:3], v[2:3]
	v_pk_mov_b32 v[48:49], v[2:3], v[2:3]
	v_pk_mov_b32 v[54:55], v[2:3], v[2:3]
	v_pk_mov_b32 v[56:57], v[2:3], v[2:3]
	v_pk_mov_b32 v[58:59], v[2:3], v[2:3]
	v_pk_mov_b32 v[60:61], v[2:3], v[2:3]
	v_pk_mov_b32 v[62:63], v[2:3], v[2:3]
	v_pk_mov_b32 v[64:65], v[2:3], v[2:3]
	v_pk_mov_b32 v[68:69], v[2:3], v[2:3]
	v_pk_mov_b32 v[70:71], v[2:3], v[2:3]
	v_pk_mov_b32 v[72:73], v[2:3], v[2:3]
	v_pk_mov_b32 v[74:75], v[2:3], v[2:3]
	v_pk_mov_b32 v[76:77], v[2:3], v[2:3]
	v_pk_mov_b32 v[78:79], v[2:3], v[2:3]
	v_pk_mov_b32 v[84:85], v[2:3], v[2:3]
	v_pk_mov_b32 v[86:87], v[2:3], v[2:3]
	v_pk_mov_b32 v[92:93], v[2:3], v[2:3]
	v_pk_mov_b32 v[94:95], v[2:3], v[2:3]
	v_pk_mov_b32 v[100:101], v[2:3], v[2:3]
	v_pk_mov_b32 v[102:103], v[2:3], v[2:3]
	v_pk_mov_b32 v[108:109], v[2:3], v[2:3]
	v_pk_mov_b32 v[110:111], v[2:3], v[2:3]
	v_pk_mov_b32 v[116:117], v[2:3], v[2:3]
	v_pk_mov_b32 v[118:119], v[2:3], v[2:3]
	v_pk_mov_b32 v[80:81], v[2:3], v[2:3]
	v_pk_mov_b32 v[82:83], v[2:3], v[2:3]
	v_pk_mov_b32 v[88:89], v[2:3], v[2:3]
	v_pk_mov_b32 v[90:91], v[2:3], v[2:3]
	v_pk_mov_b32 v[96:97], v[2:3], v[2:3]
	v_pk_mov_b32 v[98:99], v[2:3], v[2:3]
	v_pk_mov_b32 v[104:105], v[2:3], v[2:3]
	v_pk_mov_b32 v[106:107], v[2:3], v[2:3]
	v_pk_mov_b32 v[112:113], v[2:3], v[2:3]
	v_pk_mov_b32 v[114:115], v[2:3], v[2:3]
	v_pk_mov_b32 v[120:121], v[2:3], v[2:3]
	v_pk_mov_b32 v[122:123], v[2:3], v[2:3]
	v_pk_mov_b32 v[124:125], v[2:3], v[2:3]
	v_pk_mov_b32 v[126:127], v[2:3], v[2:3]
	v_pk_mov_b32 v[128:129], v[2:3], v[2:3]
	v_pk_mov_b32 v[130:131], v[2:3], v[2:3]
	s_branch .LBB0_679

.LBB0_798:
	s_add_u32 s8, s40, 0x100080
	s_addc_u32 s9, s41, 0
	s_add_u32 s70, s36, 0x100
	v_mov_b32_e32 v2, 0
	v_lshl_add_u64 v[212:213], s[8:9], 0, v[208:209]
	v_lshl_add_u64 v[214:215], s[8:9], 0, v[210:211]
	s_addc_u32 s71, s37, 0
	s_mov_b32 s8, -2
	s_mov_b64 s[58:59], 0
	s_xor_b64 s[64:65], s[64:65], -1
	v_mov_b32_e32 v3, v2
	v_pk_mov_b32 v[4:5], v[2:3], v[2:3]
	v_pk_mov_b32 v[6:7], v[2:3], v[2:3]
	v_pk_mov_b32 v[8:9], v[2:3], v[2:3]
	v_pk_mov_b32 v[18:19], v[2:3], v[2:3]
	v_pk_mov_b32 v[20:21], v[2:3], v[2:3]
	v_pk_mov_b32 v[22:23], v[2:3], v[2:3]
	v_pk_mov_b32 v[24:25], v[2:3], v[2:3]
	v_pk_mov_b32 v[34:35], v[2:3], v[2:3]
	v_pk_mov_b32 v[36:37], v[2:3], v[2:3]
	v_pk_mov_b32 v[38:39], v[2:3], v[2:3]
	v_pk_mov_b32 v[40:41], v[2:3], v[2:3]
	v_pk_mov_b32 v[50:51], v[2:3], v[2:3]
	v_pk_mov_b32 v[52:53], v[2:3], v[2:3]
	v_pk_mov_b32 v[54:55], v[2:3], v[2:3]
	v_pk_mov_b32 v[56:57], v[2:3], v[2:3]
	v_pk_mov_b32 v[10:11], v[2:3], v[2:3]
	v_pk_mov_b32 v[12:13], v[2:3], v[2:3]
	v_pk_mov_b32 v[14:15], v[2:3], v[2:3]
	v_pk_mov_b32 v[16:17], v[2:3], v[2:3]
	v_pk_mov_b32 v[26:27], v[2:3], v[2:3]
	v_pk_mov_b32 v[28:29], v[2:3], v[2:3]
	v_pk_mov_b32 v[30:31], v[2:3], v[2:3]
	v_pk_mov_b32 v[32:33], v[2:3], v[2:3]
	v_pk_mov_b32 v[42:43], v[2:3], v[2:3]
	v_pk_mov_b32 v[44:45], v[2:3], v[2:3]
	v_pk_mov_b32 v[46:47], v[2:3], v[2:3]
	v_pk_mov_b32 v[48:49], v[2:3], v[2:3]
	v_pk_mov_b32 v[58:59], v[2:3], v[2:3]
	v_pk_mov_b32 v[60:61], v[2:3], v[2:3]
	v_pk_mov_b32 v[62:63], v[2:3], v[2:3]
	v_pk_mov_b32 v[64:65], v[2:3], v[2:3]
	v_pk_mov_b32 v[68:69], v[2:3], v[2:3]
	v_pk_mov_b32 v[70:71], v[2:3], v[2:3]
	v_pk_mov_b32 v[72:73], v[2:3], v[2:3]
	v_pk_mov_b32 v[74:75], v[2:3], v[2:3]
	v_pk_mov_b32 v[84:85], v[2:3], v[2:3]
	v_pk_mov_b32 v[86:87], v[2:3], v[2:3]
	v_pk_mov_b32 v[88:89], v[2:3], v[2:3]
	v_pk_mov_b32 v[90:91], v[2:3], v[2:3]
	v_pk_mov_b32 v[100:101], v[2:3], v[2:3]
	v_pk_mov_b32 v[102:103], v[2:3], v[2:3]
	v_pk_mov_b32 v[104:105], v[2:3], v[2:3]
	v_pk_mov_b32 v[106:107], v[2:3], v[2:3]
	v_pk_mov_b32 v[116:117], v[2:3], v[2:3]
	v_pk_mov_b32 v[118:119], v[2:3], v[2:3]
	v_pk_mov_b32 v[120:121], v[2:3], v[2:3]
	v_pk_mov_b32 v[122:123], v[2:3], v[2:3]
	v_pk_mov_b32 v[76:77], v[2:3], v[2:3]
	v_pk_mov_b32 v[78:79], v[2:3], v[2:3]
	v_pk_mov_b32 v[80:81], v[2:3], v[2:3]
	v_pk_mov_b32 v[82:83], v[2:3], v[2:3]
	v_pk_mov_b32 v[92:93], v[2:3], v[2:3]
	v_pk_mov_b32 v[94:95], v[2:3], v[2:3]
	v_pk_mov_b32 v[96:97], v[2:3], v[2:3]
	v_pk_mov_b32 v[98:99], v[2:3], v[2:3]
	v_pk_mov_b32 v[108:109], v[2:3], v[2:3]
	v_pk_mov_b32 v[110:111], v[2:3], v[2:3]
	v_pk_mov_b32 v[112:113], v[2:3], v[2:3]
	v_pk_mov_b32 v[114:115], v[2:3], v[2:3]
	v_pk_mov_b32 v[124:125], v[2:3], v[2:3]
	v_pk_mov_b32 v[126:127], v[2:3], v[2:3]
	v_pk_mov_b32 v[128:129], v[2:3], v[2:3]
	v_pk_mov_b32 v[130:131], v[2:3], v[2:3]
	s_branch .LBB0_800

.LBB0_910:
	s_add_u32 s52, s52, 0x80080
	s_addc_u32 s53, s53, 0
	s_add_u32 s8, s36, 0x100
	v_mov_b32_e32 v2, 0
	s_addc_u32 s9, s37, 0
	s_mov_b32 s71, -2
	v_mov_b32_e32 v3, v2
	v_pk_mov_b32 v[4:5], v[2:3], v[2:3]
	v_pk_mov_b32 v[6:7], v[2:3], v[2:3]
	v_pk_mov_b32 v[8:9], v[2:3], v[2:3]
	v_pk_mov_b32 v[14:15], v[2:3], v[2:3]
	v_pk_mov_b32 v[16:17], v[2:3], v[2:3]
	v_pk_mov_b32 v[22:23], v[2:3], v[2:3]
	v_pk_mov_b32 v[24:25], v[2:3], v[2:3]
	v_pk_mov_b32 v[30:31], v[2:3], v[2:3]
	v_pk_mov_b32 v[32:33], v[2:3], v[2:3]
	v_pk_mov_b32 v[38:39], v[2:3], v[2:3]
	v_pk_mov_b32 v[40:41], v[2:3], v[2:3]
	v_pk_mov_b32 v[46:47], v[2:3], v[2:3]
	v_pk_mov_b32 v[48:49], v[2:3], v[2:3]
	v_pk_mov_b32 v[54:55], v[2:3], v[2:3]
	v_pk_mov_b32 v[56:57], v[2:3], v[2:3]
	v_pk_mov_b32 v[10:11], v[2:3], v[2:3]
	v_pk_mov_b32 v[12:13], v[2:3], v[2:3]
	v_pk_mov_b32 v[18:19], v[2:3], v[2:3]
	v_pk_mov_b32 v[20:21], v[2:3], v[2:3]
	v_pk_mov_b32 v[26:27], v[2:3], v[2:3]
	v_pk_mov_b32 v[28:29], v[2:3], v[2:3]
	v_pk_mov_b32 v[34:35], v[2:3], v[2:3]
	v_pk_mov_b32 v[36:37], v[2:3], v[2:3]
	v_pk_mov_b32 v[42:43], v[2:3], v[2:3]
	v_pk_mov_b32 v[44:45], v[2:3], v[2:3]
	v_pk_mov_b32 v[50:51], v[2:3], v[2:3]
	v_pk_mov_b32 v[52:53], v[2:3], v[2:3]
	v_pk_mov_b32 v[58:59], v[2:3], v[2:3]
	v_pk_mov_b32 v[60:61], v[2:3], v[2:3]
	v_pk_mov_b32 v[62:63], v[2:3], v[2:3]
	v_pk_mov_b32 v[64:65], v[2:3], v[2:3]
	v_pk_mov_b32 v[68:69], v[2:3], v[2:3]
	v_pk_mov_b32 v[70:71], v[2:3], v[2:3]
	v_pk_mov_b32 v[72:73], v[2:3], v[2:3]
	v_pk_mov_b32 v[74:75], v[2:3], v[2:3]
	v_pk_mov_b32 v[80:81], v[2:3], v[2:3]
	v_pk_mov_b32 v[82:83], v[2:3], v[2:3]
	v_pk_mov_b32 v[88:89], v[2:3], v[2:3]
	v_pk_mov_b32 v[90:91], v[2:3], v[2:3]
	v_pk_mov_b32 v[96:97], v[2:3], v[2:3]
	v_pk_mov_b32 v[98:99], v[2:3], v[2:3]
	v_pk_mov_b32 v[104:105], v[2:3], v[2:3]
	v_pk_mov_b32 v[106:107], v[2:3], v[2:3]
	v_pk_mov_b32 v[112:113], v[2:3], v[2:3]
	v_pk_mov_b32 v[114:115], v[2:3], v[2:3]
	v_pk_mov_b32 v[120:121], v[2:3], v[2:3]
	v_pk_mov_b32 v[122:123], v[2:3], v[2:3]
	v_pk_mov_b32 v[76:77], v[2:3], v[2:3]
	v_pk_mov_b32 v[78:79], v[2:3], v[2:3]
	v_pk_mov_b32 v[84:85], v[2:3], v[2:3]
	v_pk_mov_b32 v[86:87], v[2:3], v[2:3]
	v_pk_mov_b32 v[92:93], v[2:3], v[2:3]
	v_pk_mov_b32 v[94:95], v[2:3], v[2:3]
	v_pk_mov_b32 v[100:101], v[2:3], v[2:3]
	v_pk_mov_b32 v[102:103], v[2:3], v[2:3]
	v_pk_mov_b32 v[108:109], v[2:3], v[2:3]
	v_pk_mov_b32 v[110:111], v[2:3], v[2:3]
	v_pk_mov_b32 v[116:117], v[2:3], v[2:3]
	v_pk_mov_b32 v[118:119], v[2:3], v[2:3]
	v_pk_mov_b32 v[124:125], v[2:3], v[2:3]
	v_pk_mov_b32 v[126:127], v[2:3], v[2:3]
	v_pk_mov_b32 v[128:129], v[2:3], v[2:3]
	v_pk_mov_b32 v[130:131], v[2:3], v[2:3]

.LBB0_926:
	s_add_u32 s50, s50, 0x40080
	s_addc_u32 s51, s51, 0
	s_add_u32 s8, s36, 0x100
	v_mov_b32_e32 v2, 0
	s_addc_u32 s9, s37, 0
	s_mov_b32 s67, -2
	v_mov_b32_e32 v3, v2
	v_pk_mov_b32 v[4:5], v[2:3], v[2:3]
	v_pk_mov_b32 v[6:7], v[2:3], v[2:3]
	v_pk_mov_b32 v[8:9], v[2:3], v[2:3]
	v_pk_mov_b32 v[18:19], v[2:3], v[2:3]
	v_pk_mov_b32 v[20:21], v[2:3], v[2:3]
	v_pk_mov_b32 v[22:23], v[2:3], v[2:3]
	v_pk_mov_b32 v[24:25], v[2:3], v[2:3]
	v_pk_mov_b32 v[34:35], v[2:3], v[2:3]
	v_pk_mov_b32 v[36:37], v[2:3], v[2:3]
	v_pk_mov_b32 v[38:39], v[2:3], v[2:3]
	v_pk_mov_b32 v[40:41], v[2:3], v[2:3]
	v_pk_mov_b32 v[50:51], v[2:3], v[2:3]
	v_pk_mov_b32 v[52:53], v[2:3], v[2:3]
	v_pk_mov_b32 v[54:55], v[2:3], v[2:3]
	v_pk_mov_b32 v[56:57], v[2:3], v[2:3]
	v_pk_mov_b32 v[10:11], v[2:3], v[2:3]
	v_pk_mov_b32 v[12:13], v[2:3], v[2:3]
	v_pk_mov_b32 v[14:15], v[2:3], v[2:3]
	v_pk_mov_b32 v[16:17], v[2:3], v[2:3]
	v_pk_mov_b32 v[26:27], v[2:3], v[2:3]
	v_pk_mov_b32 v[28:29], v[2:3], v[2:3]
	v_pk_mov_b32 v[30:31], v[2:3], v[2:3]
	v_pk_mov_b32 v[32:33], v[2:3], v[2:3]
	v_pk_mov_b32 v[42:43], v[2:3], v[2:3]
	v_pk_mov_b32 v[44:45], v[2:3], v[2:3]
	v_pk_mov_b32 v[46:47], v[2:3], v[2:3]
	v_pk_mov_b32 v[48:49], v[2:3], v[2:3]
	v_pk_mov_b32 v[58:59], v[2:3], v[2:3]
	v_pk_mov_b32 v[60:61], v[2:3], v[2:3]
	v_pk_mov_b32 v[62:63], v[2:3], v[2:3]
	v_pk_mov_b32 v[64:65], v[2:3], v[2:3]
	v_pk_mov_b32 v[68:69], v[2:3], v[2:3]
	v_pk_mov_b32 v[70:71], v[2:3], v[2:3]
	v_pk_mov_b32 v[72:73], v[2:3], v[2:3]
	v_pk_mov_b32 v[74:75], v[2:3], v[2:3]
	v_pk_mov_b32 v[84:85], v[2:3], v[2:3]
	v_pk_mov_b32 v[86:87], v[2:3], v[2:3]
	v_pk_mov_b32 v[88:89], v[2:3], v[2:3]
	v_pk_mov_b32 v[90:91], v[2:3], v[2:3]
	v_pk_mov_b32 v[100:101], v[2:3], v[2:3]
	v_pk_mov_b32 v[102:103], v[2:3], v[2:3]
	v_pk_mov_b32 v[104:105], v[2:3], v[2:3]
	v_pk_mov_b32 v[106:107], v[2:3], v[2:3]
	v_pk_mov_b32 v[116:117], v[2:3], v[2:3]
	v_pk_mov_b32 v[118:119], v[2:3], v[2:3]
	v_pk_mov_b32 v[120:121], v[2:3], v[2:3]
	v_pk_mov_b32 v[122:123], v[2:3], v[2:3]
	v_pk_mov_b32 v[76:77], v[2:3], v[2:3]
	v_pk_mov_b32 v[78:79], v[2:3], v[2:3]
	v_pk_mov_b32 v[80:81], v[2:3], v[2:3]
	v_pk_mov_b32 v[82:83], v[2:3], v[2:3]
	v_pk_mov_b32 v[92:93], v[2:3], v[2:3]
	v_pk_mov_b32 v[94:95], v[2:3], v[2:3]
	v_pk_mov_b32 v[96:97], v[2:3], v[2:3]
	v_pk_mov_b32 v[98:99], v[2:3], v[2:3]
	v_pk_mov_b32 v[108:109], v[2:3], v[2:3]
	v_pk_mov_b32 v[110:111], v[2:3], v[2:3]
	v_pk_mov_b32 v[112:113], v[2:3], v[2:3]
	v_pk_mov_b32 v[114:115], v[2:3], v[2:3]
	v_pk_mov_b32 v[124:125], v[2:3], v[2:3]
	v_pk_mov_b32 v[126:127], v[2:3], v[2:3]
	v_pk_mov_b32 v[128:129], v[2:3], v[2:3]
	v_pk_mov_b32 v[130:131], v[2:3], v[2:3]

.LBB0_997:
	s_add_u32 s34, s34, 0x40080
	s_addc_u32 s35, s35, 0
	s_add_u32 s8, s36, 0x100
	v_mov_b32_e32 v2, 0
	s_addc_u32 s9, s37, 0
	s_mov_b32 s26, -2
	v_mov_b32_e32 v3, v2
	v_pk_mov_b32 v[4:5], v[2:3], v[2:3]
	v_pk_mov_b32 v[6:7], v[2:3], v[2:3]
	v_pk_mov_b32 v[8:9], v[2:3], v[2:3]
	v_pk_mov_b32 v[18:19], v[2:3], v[2:3]
	v_pk_mov_b32 v[20:21], v[2:3], v[2:3]
	v_pk_mov_b32 v[22:23], v[2:3], v[2:3]
	v_pk_mov_b32 v[24:25], v[2:3], v[2:3]
	v_pk_mov_b32 v[34:35], v[2:3], v[2:3]
	v_pk_mov_b32 v[36:37], v[2:3], v[2:3]
	v_pk_mov_b32 v[38:39], v[2:3], v[2:3]
	v_pk_mov_b32 v[40:41], v[2:3], v[2:3]
	v_pk_mov_b32 v[50:51], v[2:3], v[2:3]
	v_pk_mov_b32 v[52:53], v[2:3], v[2:3]
	v_pk_mov_b32 v[54:55], v[2:3], v[2:3]
	v_pk_mov_b32 v[56:57], v[2:3], v[2:3]
	v_pk_mov_b32 v[10:11], v[2:3], v[2:3]
	v_pk_mov_b32 v[12:13], v[2:3], v[2:3]
	v_pk_mov_b32 v[14:15], v[2:3], v[2:3]
	v_pk_mov_b32 v[16:17], v[2:3], v[2:3]
	v_pk_mov_b32 v[26:27], v[2:3], v[2:3]
	v_pk_mov_b32 v[28:29], v[2:3], v[2:3]
	v_pk_mov_b32 v[30:31], v[2:3], v[2:3]
	v_pk_mov_b32 v[32:33], v[2:3], v[2:3]
	v_pk_mov_b32 v[42:43], v[2:3], v[2:3]
	v_pk_mov_b32 v[44:45], v[2:3], v[2:3]
	v_pk_mov_b32 v[46:47], v[2:3], v[2:3]
	v_pk_mov_b32 v[48:49], v[2:3], v[2:3]
	v_pk_mov_b32 v[76:77], v[2:3], v[2:3]
	v_pk_mov_b32 v[78:79], v[2:3], v[2:3]
	v_pk_mov_b32 v[80:81], v[2:3], v[2:3]
	v_pk_mov_b32 v[82:83], v[2:3], v[2:3]
	v_pk_mov_b32 v[100:101], v[2:3], v[2:3]
	v_pk_mov_b32 v[102:103], v[2:3], v[2:3]
	v_pk_mov_b32 v[104:105], v[2:3], v[2:3]
	v_pk_mov_b32 v[106:107], v[2:3], v[2:3]
	v_pk_mov_b32 v[116:117], v[2:3], v[2:3]
	v_pk_mov_b32 v[118:119], v[2:3], v[2:3]
	v_pk_mov_b32 v[120:121], v[2:3], v[2:3]
	v_pk_mov_b32 v[122:123], v[2:3], v[2:3]
	v_pk_mov_b32 v[132:133], v[2:3], v[2:3]
	v_pk_mov_b32 v[134:135], v[2:3], v[2:3]
	v_pk_mov_b32 v[136:137], v[2:3], v[2:3]
	v_pk_mov_b32 v[138:139], v[2:3], v[2:3]
	v_pk_mov_b32 v[148:149], v[2:3], v[2:3]
	v_pk_mov_b32 v[150:151], v[2:3], v[2:3]
	v_pk_mov_b32 v[152:153], v[2:3], v[2:3]
	v_pk_mov_b32 v[154:155], v[2:3], v[2:3]
	v_pk_mov_b32 v[108:109], v[2:3], v[2:3]
	v_pk_mov_b32 v[110:111], v[2:3], v[2:3]
	v_pk_mov_b32 v[112:113], v[2:3], v[2:3]
	v_pk_mov_b32 v[114:115], v[2:3], v[2:3]
	v_pk_mov_b32 v[124:125], v[2:3], v[2:3]
	v_pk_mov_b32 v[126:127], v[2:3], v[2:3]
	v_pk_mov_b32 v[128:129], v[2:3], v[2:3]
	v_pk_mov_b32 v[130:131], v[2:3], v[2:3]
	v_pk_mov_b32 v[140:141], v[2:3], v[2:3]
	v_pk_mov_b32 v[142:143], v[2:3], v[2:3]
	v_pk_mov_b32 v[144:145], v[2:3], v[2:3]
	v_pk_mov_b32 v[146:147], v[2:3], v[2:3]
	v_pk_mov_b32 v[156:157], v[2:3], v[2:3]
	v_pk_mov_b32 v[158:159], v[2:3], v[2:3]
	v_pk_mov_b32 v[160:161], v[2:3], v[2:3]
	v_pk_mov_b32 v[162:163], v[2:3], v[2:3]

.LBB0_1237:
	v_mov_b32_e32 v209, v67
	v_mov_b32_e32 v213, v67
	s_mov_b64 s[8:9], 0x100
	v_mov_b32_e32 v50, 0
	v_lshl_add_u64 v[216:217], s[48:49], 0, v[212:213]
	v_lshl_add_u64 v[218:219], s[48:49], 0, v[208:209]
	v_lshl_add_u64 v[220:221], v[2:3], 0, s[8:9]
	s_mov_b32 s45, -2
	s_mov_b64 s[36:37], 0
	s_xor_b64 s[34:35], s[34:35], -1
	v_mov_b32_e32 v51, v50
	v_pk_mov_b32 v[52:53], v[50:51], v[50:51]
	v_pk_mov_b32 v[58:59], v[50:51], v[50:51]
	v_pk_mov_b32 v[60:61], v[50:51], v[50:51]
	v_pk_mov_b32 v[2:3], v[50:51], v[50:51]
	v_pk_mov_b32 v[4:5], v[50:51], v[50:51]
	v_pk_mov_b32 v[6:7], v[50:51], v[50:51]
	v_pk_mov_b32 v[8:9], v[50:51], v[50:51]
	v_pk_mov_b32 v[18:19], v[50:51], v[50:51]
	v_pk_mov_b32 v[20:21], v[50:51], v[50:51]
	v_pk_mov_b32 v[22:23], v[50:51], v[50:51]
	v_pk_mov_b32 v[24:25], v[50:51], v[50:51]
	v_pk_mov_b32 v[34:35], v[50:51], v[50:51]
	v_pk_mov_b32 v[36:37], v[50:51], v[50:51]
	v_pk_mov_b32 v[38:39], v[50:51], v[50:51]
	v_pk_mov_b32 v[40:41], v[50:51], v[50:51]
	v_pk_mov_b32 v[54:55], v[50:51], v[50:51]
	v_pk_mov_b32 v[56:57], v[50:51], v[50:51]
	v_pk_mov_b32 v[62:63], v[50:51], v[50:51]
	v_pk_mov_b32 v[64:65], v[50:51], v[50:51]
	v_pk_mov_b32 v[68:69], v[50:51], v[50:51]
	v_pk_mov_b32 v[70:71], v[50:51], v[50:51]
	v_pk_mov_b32 v[76:77], v[50:51], v[50:51]
	v_pk_mov_b32 v[78:79], v[50:51], v[50:51]
	v_pk_mov_b32 v[84:85], v[50:51], v[50:51]
	v_pk_mov_b32 v[86:87], v[50:51], v[50:51]
	v_pk_mov_b32 v[92:93], v[50:51], v[50:51]
	v_pk_mov_b32 v[94:95], v[50:51], v[50:51]
	v_pk_mov_b32 v[100:101], v[50:51], v[50:51]
	v_pk_mov_b32 v[102:103], v[50:51], v[50:51]
	v_pk_mov_b32 v[108:109], v[50:51], v[50:51]
	v_pk_mov_b32 v[110:111], v[50:51], v[50:51]
	v_pk_mov_b32 v[116:117], v[50:51], v[50:51]
	v_pk_mov_b32 v[118:119], v[50:51], v[50:51]
	v_pk_mov_b32 v[124:125], v[50:51], v[50:51]
	v_pk_mov_b32 v[126:127], v[50:51], v[50:51]
	v_pk_mov_b32 v[72:73], v[50:51], v[50:51]
	v_pk_mov_b32 v[74:75], v[50:51], v[50:51]
	v_pk_mov_b32 v[80:81], v[50:51], v[50:51]
	v_pk_mov_b32 v[82:83], v[50:51], v[50:51]
	v_pk_mov_b32 v[88:89], v[50:51], v[50:51]
	v_pk_mov_b32 v[90:91], v[50:51], v[50:51]
	v_pk_mov_b32 v[96:97], v[50:51], v[50:51]
	v_pk_mov_b32 v[98:99], v[50:51], v[50:51]
	v_pk_mov_b32 v[104:105], v[50:51], v[50:51]
	v_pk_mov_b32 v[106:107], v[50:51], v[50:51]
	v_pk_mov_b32 v[112:113], v[50:51], v[50:51]
	v_pk_mov_b32 v[114:115], v[50:51], v[50:51]
	v_pk_mov_b32 v[120:121], v[50:51], v[50:51]
	v_pk_mov_b32 v[122:123], v[50:51], v[50:51]
	v_pk_mov_b32 v[128:129], v[50:51], v[50:51]
	v_pk_mov_b32 v[130:131], v[50:51], v[50:51]
	v_pk_mov_b32 v[46:47], v[50:51], v[50:51]
	v_pk_mov_b32 v[48:49], v[50:51], v[50:51]
	v_pk_mov_b32 v[42:43], v[50:51], v[50:51]
	v_pk_mov_b32 v[44:45], v[50:51], v[50:51]
	v_pk_mov_b32 v[30:31], v[50:51], v[50:51]
	v_pk_mov_b32 v[32:33], v[50:51], v[50:51]
	v_pk_mov_b32 v[26:27], v[50:51], v[50:51]
	v_pk_mov_b32 v[28:29], v[50:51], v[50:51]
	v_pk_mov_b32 v[14:15], v[50:51], v[50:51]
	v_pk_mov_b32 v[16:17], v[50:51], v[50:51]
	v_pk_mov_b32 v[10:11], v[50:51], v[50:51]
	v_pk_mov_b32 v[12:13], v[50:51], v[50:51]
	s_branch .LBB0_1239

.LBB0_1478:
	s_add_u32 s8, s74, 0x20080
	s_addc_u32 s9, s75, 0
	v_lshl_add_u64 v[214:215], s[8:9], 0, v[208:209]
	v_lshl_add_u64 v[216:217], s[8:9], 0, v[210:211]
	s_mov_b64 s[8:9], 0x100
	v_lshl_add_u64 v[218:219], v[2:3], 0, s[8:9]
	v_mov_b32_e32 v2, 0
	s_mov_b32 s8, -2
	s_mov_b64 s[84:85], 0
	s_xor_b64 s[86:87], s[36:37], -1
	v_mov_b32_e32 v3, v2
	v_pk_mov_b32 v[4:5], v[2:3], v[2:3]
	v_pk_mov_b32 v[6:7], v[2:3], v[2:3]
	v_pk_mov_b32 v[8:9], v[2:3], v[2:3]
	v_pk_mov_b32 v[14:15], v[2:3], v[2:3]
	v_pk_mov_b32 v[16:17], v[2:3], v[2:3]
	v_pk_mov_b32 v[22:23], v[2:3], v[2:3]
	v_pk_mov_b32 v[24:25], v[2:3], v[2:3]
	v_pk_mov_b32 v[30:31], v[2:3], v[2:3]
	v_pk_mov_b32 v[32:33], v[2:3], v[2:3]
	v_pk_mov_b32 v[38:39], v[2:3], v[2:3]
	v_pk_mov_b32 v[40:41], v[2:3], v[2:3]
	v_pk_mov_b32 v[46:47], v[2:3], v[2:3]
	v_pk_mov_b32 v[48:49], v[2:3], v[2:3]
	v_pk_mov_b32 v[54:55], v[2:3], v[2:3]
	v_pk_mov_b32 v[56:57], v[2:3], v[2:3]
	v_pk_mov_b32 v[10:11], v[2:3], v[2:3]
	v_pk_mov_b32 v[12:13], v[2:3], v[2:3]
	v_pk_mov_b32 v[18:19], v[2:3], v[2:3]
	v_pk_mov_b32 v[20:21], v[2:3], v[2:3]
	v_pk_mov_b32 v[26:27], v[2:3], v[2:3]
	v_pk_mov_b32 v[28:29], v[2:3], v[2:3]
	v_pk_mov_b32 v[34:35], v[2:3], v[2:3]
	v_pk_mov_b32 v[36:37], v[2:3], v[2:3]
	v_pk_mov_b32 v[42:43], v[2:3], v[2:3]
	v_pk_mov_b32 v[44:45], v[2:3], v[2:3]
	v_pk_mov_b32 v[50:51], v[2:3], v[2:3]
	v_pk_mov_b32 v[52:53], v[2:3], v[2:3]
	v_pk_mov_b32 v[58:59], v[2:3], v[2:3]
	v_pk_mov_b32 v[60:61], v[2:3], v[2:3]
	v_pk_mov_b32 v[62:63], v[2:3], v[2:3]
	v_pk_mov_b32 v[64:65], v[2:3], v[2:3]
	v_pk_mov_b32 v[68:69], v[2:3], v[2:3]
	v_pk_mov_b32 v[70:71], v[2:3], v[2:3]
	v_pk_mov_b32 v[72:73], v[2:3], v[2:3]
	v_pk_mov_b32 v[74:75], v[2:3], v[2:3]
	v_pk_mov_b32 v[80:81], v[2:3], v[2:3]
	v_pk_mov_b32 v[82:83], v[2:3], v[2:3]
	v_pk_mov_b32 v[88:89], v[2:3], v[2:3]
	v_pk_mov_b32 v[90:91], v[2:3], v[2:3]
	v_pk_mov_b32 v[96:97], v[2:3], v[2:3]
	v_pk_mov_b32 v[98:99], v[2:3], v[2:3]
	v_pk_mov_b32 v[104:105], v[2:3], v[2:3]
	v_pk_mov_b32 v[106:107], v[2:3], v[2:3]
	v_pk_mov_b32 v[112:113], v[2:3], v[2:3]
	v_pk_mov_b32 v[114:115], v[2:3], v[2:3]
	v_pk_mov_b32 v[120:121], v[2:3], v[2:3]
	v_pk_mov_b32 v[122:123], v[2:3], v[2:3]
	v_pk_mov_b32 v[76:77], v[2:3], v[2:3]
	v_pk_mov_b32 v[78:79], v[2:3], v[2:3]
	v_pk_mov_b32 v[84:85], v[2:3], v[2:3]
	v_pk_mov_b32 v[86:87], v[2:3], v[2:3]
	v_pk_mov_b32 v[92:93], v[2:3], v[2:3]
	v_pk_mov_b32 v[94:95], v[2:3], v[2:3]
	v_pk_mov_b32 v[100:101], v[2:3], v[2:3]
	v_pk_mov_b32 v[102:103], v[2:3], v[2:3]
	v_pk_mov_b32 v[108:109], v[2:3], v[2:3]
	v_pk_mov_b32 v[110:111], v[2:3], v[2:3]
	v_pk_mov_b32 v[116:117], v[2:3], v[2:3]
	v_pk_mov_b32 v[118:119], v[2:3], v[2:3]
	v_pk_mov_b32 v[124:125], v[2:3], v[2:3]
	v_pk_mov_b32 v[126:127], v[2:3], v[2:3]
	v_pk_mov_b32 v[128:129], v[2:3], v[2:3]
	v_pk_mov_b32 v[130:131], v[2:3], v[2:3]
	s_branch .LBB0_1480
